# DIFF loop: first QK MFMA of the iteration issued right behind the barrier (before the K/V DMA issue); rest as previous version
# speedup vs baseline: 1.0113x; 1.0058x over previous
.LBB0_953:
	v_mfma_f32_32x32x16_bf16 v[114:129], v[98:101], v[130:133], 0
	s_min_i32 s28, s26, 0x101
	s_lshl_b32 s28, s28, 13
	s_add_i32 s88, s28, 0x4000
	s_lshl_b32 s28, s22, 14
	s_add_i32 s28, s21, s28
	v_lshl_add_u64 v[106:107], v[174:175], 0, s[88:89]
	s_mov_b32 m0, s28
	v_lshl_add_u32 v181, s27, 14, v0
	global_load_lds_dwordx4 v[106:107], off
	v_lshl_add_u64 v[106:107], v[176:177], 0, s[88:89]
	s_add_i32 m0, s28, 0x2000
	s_lshl_b32 s28, s25, 14
	global_load_lds_dwordx4 v[106:107], off
	ds_read_b128 v[190:193], v181 offset:12288
	v_add_u32_e32 v189, s28, v0
	v_lshl_add_u32 v210, s23, 14, v188
	v_exp_f32_e32 v194, v82
	v_exp_f32_e32 v196, v83
	v_exp_f32_e32 v198, v84
	v_exp_f32_e32 v200, v85
	v_mfma_f32_32x32x16_bf16 v[98:113], v[102:105], v[134:137], 0
	ds_read_b128 v[82:85], v181 offset:12800
	v_cvt_pk_bf16_f32 v170, v194, v196
	v_cvt_pk_bf16_f32 v171, v198, v200
	v_exp_f32_e32 v202, v86
	v_exp_f32_e32 v204, v87
	s_waitcnt lgkmcnt(0)
	v_mfma_f32_32x32x16_bf16 v[114:129], v[162:165], v[138:141], v[114:129]
	v_cvt_pk_bf16_f32 v172, v202, v204
	v_exp_f32_e32 v206, v88
	v_exp_f32_e32 v208, v89
	v_mfma_f32_32x32x16_bf16 v[98:113], v[166:169], v[142:145], v[98:113]
	v_exp_f32_e32 v168, v92
	v_exp_f32_e32 v166, v93
	v_cvt_pk_bf16_f32 v173, v206, v208
	v_exp_f32_e32 v214, v90
	v_exp_f32_e32 v216, v91
	v_mfma_f32_32x32x16_bf16 v[34:49], v[190:193], v[150:153], v[34:49]
	ds_read_b128 v[86:89], v181 offset:14336
	v_cvt_pk_bf16_f32 v162, v214, v216
	v_cvt_pk_bf16_f32 v163, v168, v166
	v_exp_f32_e32 v182, v94
	v_exp_f32_e32 v180, v95
	v_mfma_f32_32x32x16_bf16 v[50:65], v[82:85], v[150:153], v[50:65]
	ds_read_b128 v[90:93], v181 offset:14848
	v_cvt_pk_bf16_f32 v164, v182, v180
	v_exp_f32_e32 v186, v96
	v_exp_f32_e32 v184, v97
	v_mfma_f32_32x32x16_bf16 v[2:17], v[190:193], v[158:161], v[2:17]
	v_cvt_pk_bf16_f32 v165, v186, v184
	v_exp_f32_e32 v195, v66
	v_exp_f32_e32 v197, v67
	v_exp_f32_e32 v199, v68
	v_exp_f32_e32 v201, v69
	v_mfma_f32_32x32x16_bf16 v[18:33], v[82:85], v[158:161], v[18:33]
	v_cvt_pk_bf16_f32 v158, v195, v197
	v_cvt_pk_bf16_f32 v159, v199, v201
	v_exp_f32_e32 v203, v70
	v_exp_f32_e32 v205, v71
	s_waitcnt lgkmcnt(0)
	v_mfma_f32_32x32x16_bf16 v[34:49], v[86:89], v[154:157], v[34:49]
	ds_read_b128 v[66:69], v210
	v_cvt_pk_bf16_f32 v160, v203, v205
	v_exp_f32_e32 v207, v72
	v_exp_f32_e32 v209, v73
	v_mfma_f32_32x32x16_bf16 v[50:65], v[90:93], v[154:157], v[50:65]
	ds_read_b128 v[70:73], v210 offset:4096
	v_exp_f32_e32 v169, v76
	v_exp_f32_e32 v167, v77
	v_cvt_pk_bf16_f32 v161, v207, v209
	v_exp_f32_e32 v215, v74
	v_exp_f32_e32 v217, v75
	v_pk_add_f32 v[74:75], v[178:179], v[194:195]
	v_mfma_f32_32x32x16_bf16 v[2:17], v[86:89], v[146:149], v[2:17]
	v_add_f32_e64 v74, v196, v74
	v_add_f32_e64 v75, v197, v75
	ds_read_b128 v[152:155], v210 offset:2048
	v_add_f32_e64 v74, v198, v74
	v_add_f32_e64 v75, v199, v75
	v_cvt_pk_bf16_f32 v190, v215, v217
	v_pk_add_f32 v[234:235], v[200:201], v[234:235]
	v_cvt_pk_bf16_f32 v191, v169, v167
	v_pk_add_f32 v[74:75], v[202:203], v[74:75]
	v_exp_f32_e32 v183, v78
	v_pk_add_f32 v[234:235], v[204:205], v[234:235]
	v_exp_f32_e32 v181, v79
	v_pk_add_f32 v[74:75], v[206:207], v[74:75]
	v_pk_add_f32 v[234:235], v[208:209], v[234:235]
	v_pk_add_f32 v[74:75], v[214:215], v[74:75]
	s_nop 0
	v_pk_add_f32 v[178:179], v[216:217], v[74:75]
	v_mfma_f32_32x32x16_bf16 v[18:33], v[90:93], v[146:149], v[18:33]
	v_exp_f32_e32 v187, v80
	v_exp_f32_e32 v185, v81
	ds_read_b128 v[194:197], v210 offset:6144
	v_cvt_pk_bf16_f32 v192, v183, v181
	v_cvt_pk_bf16_f32 v193, v187, v185
	s_waitcnt lgkmcnt(0)
	v_mfma_f32_32x32x16_bf16 v[82:97], v[66:69], v[130:133], 0
	ds_read_b128 v[146:149], v189 offset:8192
	v_exp_f32_e32 v198, v114
	v_exp_f32_e32 v200, v115
	v_exp_f32_e32 v202, v116
	v_exp_f32_e32 v204, v117
	v_mfma_f32_32x32x16_bf16 v[66:81], v[70:73], v[134:137], 0
	ds_read_b128 v[114:117], v189 offset:8704
	v_cvt_pk_bf16_f32 v150, v198, v200
	v_cvt_pk_bf16_f32 v151, v202, v204
	v_exp_f32_e32 v206, v118
	v_exp_f32_e32 v208, v119
	v_mfma_f32_32x32x16_bf16 v[82:97], v[152:155], v[138:141], v[82:97]
	v_cvt_pk_bf16_f32 v152, v206, v208
	v_exp_f32_e32 v214, v120
	v_exp_f32_e32 v216, v121
	v_mfma_f32_32x32x16_bf16 v[66:81], v[194:197], v[142:145], v[66:81]
	v_cvt_pk_bf16_f32 v153, v214, v216
	v_exp_f32_e32 v194, v122
	v_exp_f32_e32 v196, v123
	v_exp_f32_e32 v218, v124
	v_exp_f32_e32 v220, v125
	s_waitcnt lgkmcnt(0)
	v_mfma_f32_32x32x16_bf16 v[34:49], v[146:149], v[170:173], v[34:49]
	ds_read_b128 v[118:121], v189 offset:10240
	v_cvt_pk_bf16_f32 v154, v194, v196
	v_cvt_pk_bf16_f32 v155, v218, v220
	v_exp_f32_e32 v126, v126
	v_exp_f32_e32 v222, v127
	v_mfma_f32_32x32x16_bf16 v[50:65], v[114:117], v[170:173], v[50:65]
	ds_read_b128 v[122:125], v189 offset:10752
	v_cvt_pk_bf16_f32 v156, v126, v222
	v_exp_f32_e32 v128, v128
	v_exp_f32_e32 v170, v129
	v_mfma_f32_32x32x16_bf16 v[2:17], v[146:149], v[158:161], v[2:17]
	v_cvt_pk_bf16_f32 v157, v128, v170
	v_exp_f32_e32 v199, v98
	v_exp_f32_e32 v201, v99
	v_exp_f32_e32 v203, v100
	v_exp_f32_e32 v205, v101
	v_mfma_f32_32x32x16_bf16 v[18:33], v[114:117], v[158:161], v[18:33]
	v_cvt_pk_bf16_f32 v158, v199, v201
	v_cvt_pk_bf16_f32 v159, v203, v205
	v_exp_f32_e32 v207, v102
	v_exp_f32_e32 v209, v103
	v_pk_add_f32 v[102:103], v[168:169], v[178:179]
	s_waitcnt lgkmcnt(0)
	v_mfma_f32_32x32x16_bf16 v[34:49], v[118:121], v[162:165], v[34:49]
	v_add_f32_e64 v102, v166, v102
	v_add_f32_e64 v103, v167, v103
	ds_read_b128 v[98:101], v210 offset:512
	v_add_f32_e64 v102, v182, v102
	v_add_f32_e64 v103, v183, v103
	v_cvt_pk_bf16_f32 v160, v207, v209
	v_pk_add_f32 v[234:235], v[180:181], v[234:235]
	v_exp_f32_e32 v215, v104
	v_pk_add_f32 v[102:103], v[186:187], v[102:103]
	v_exp_f32_e32 v217, v105
	v_pk_add_f32 v[234:235], v[184:185], v[234:235]
	v_pk_add_f32 v[102:103], v[102:103], v[198:199]
	v_pk_add_f32 v[234:235], v[200:201], v[234:235]
	v_pk_add_f32 v[102:103], v[202:203], v[102:103]
	v_pk_add_f32 v[234:235], v[204:205], v[234:235]
	v_pk_add_f32 v[114:115], v[206:207], v[102:103]
	v_mfma_f32_32x32x16_bf16 v[50:65], v[122:125], v[162:165], v[50:65]
	ds_read_b128 v[102:105], v210 offset:4608
	v_cvt_pk_bf16_f32 v161, v215, v217
	v_exp_f32_e32 v195, v106
	v_exp_f32_e32 v197, v107
	v_exp_f32_e32 v219, v108
	v_exp_f32_e32 v221, v109
	v_mfma_f32_32x32x16_bf16 v[2:17], v[118:121], v[190:193], v[2:17]
	ds_read_b128 v[162:165], v210 offset:2560
	v_cvt_pk_bf16_f32 v146, v195, v197
	v_cvt_pk_bf16_f32 v147, v219, v221
	v_exp_f32_e32 v127, v110
	v_exp_f32_e32 v223, v111
	v_pk_add_f32 v[106:107], v[208:209], v[114:115]
	v_mfma_f32_32x32x16_bf16 v[18:33], v[122:125], v[190:193], v[18:33]
	v_add_f32_e64 v106, v214, v106
	v_add_f32_e64 v107, v215, v107
	v_exp_f32_e32 v129, v112
	v_pk_add_f32 v[106:107], v[216:217], v[106:107]
	ds_read_b128 v[166:169], v210 offset:6656
	v_pk_add_f32 v[234:235], v[194:195], v[234:235]
	v_exp_f32_e32 v171, v113
	v_pk_add_f32 v[106:107], v[196:197], v[106:107]
	v_cvt_pk_bf16_f32 v148, v127, v223
	v_pk_add_f32 v[234:235], v[218:219], v[234:235]
	v_cvt_pk_bf16_f32 v149, v129, v171
	v_pk_add_f32 v[106:107], v[220:221], v[106:107]
	v_pk_add_f32 v[234:235], v[126:127], v[234:235]
	v_pk_add_f32 v[106:107], v[222:223], v[106:107]
	v_pk_add_f32 v[234:235], v[128:129], v[234:235]
	v_pk_add_f32 v[178:179], v[170:171], v[106:107]
	s_add_i32 s27, s22, 1
	s_waitcnt vmcnt(0)
	s_and_b32 s28, s27, 3
	s_add_i32 s26, s26, 1
	s_cmpk_eq_i32 s26, 0x104
	s_mov_b32 s27, s25
	s_mov_b32 s25, s23
	s_mov_b32 s23, s22
	s_mov_b32 s22, s28
	s_waitcnt vmcnt(0) lgkmcnt(0)
	s_barrier
	s_cbranch_scc0 .LBB0_953
	v_add_f32_e32 v178, v178, v234
	v_add_f32_e32 v179, v179, v235
	ds_read_b128 v[66:69], v189 offset:12288
	ds_read_b128 v[70:73], v189 offset:12800
	v_mov_b32_e32 v0, v230
	s_waitcnt lgkmcnt(1)
	v_mfma_f32_32x32x16_bf16 v[34:49], v[66:69], v[150:153], v[34:49]
	s_waitcnt lgkmcnt(0)
	v_mfma_f32_32x32x16_bf16 v[50:65], v[70:73], v[150:153], v[50:65]
	v_mfma_f32_32x32x16_bf16 v[2:17], v[66:69], v[158:161], v[2:17]
	v_mfma_f32_32x32x16_bf16 v[18:33], v[70:73], v[158:161], v[18:33]
	ds_read_b128 v[68:71], v189 offset:14336
	ds_read_b128 v[72:75], v189 offset:14848
	v_mbcnt_lo_u32_b32 v76, -1, 0
	v_mbcnt_hi_u32_b32 v76, -1, v76
	v_mbcnt_lo_u32_b32 v77, -1, 0
	v_mbcnt_hi_u32_b32 v77, -1, v77
	global_load_dwordx2 v[66:67], v1, s[6:7]
	v_lshlrev_b32_e32 v77, 2, v77
	v_xor_b32_e32 v77, 0x80, v77
	v_lshlrev_b32_e32 v76, 2, v76
	ds_bpermute_b32 v77, v77, v179
	v_xor_b32_e32 v76, 0x80, v76
	ds_bpermute_b32 v76, v76, v178
	s_waitcnt lgkmcnt(3)
	v_mfma_f32_32x32x16_bf16 v[2:17], v[68:71], v[146:149], v[2:17]
	v_readfirstlane_b32 s21, v0
	s_ashr_i32 s21, s21, 1
	s_andn2_b32 s21, s21, 31
	s_cmpk_lt_i32 s21, 0x100
	s_waitcnt lgkmcnt(2)
	v_mfma_f32_32x32x16_bf16 v[18:33], v[72:75], v[146:149], v[18:33]
	v_mfma_f32_32x32x16_bf16 v[34:49], v[68:71], v[154:157], v[34:49]
	s_waitcnt lgkmcnt(1)
	v_add_f32_e32 v70, v179, v77
	v_mbcnt_lo_u32_b32 v68, -1, 0
	v_mbcnt_hi_u32_b32 v68, -1, v68
	v_rcp_f32_e32 v70, v70
	v_lshlrev_b32_e32 v69, 2, v68
	s_waitcnt lgkmcnt(0)
	v_add_f32_e32 v68, v178, v76
	v_rcp_f32_e32 v68, v68
	s_waitcnt vmcnt(0)
	v_mul_f32_e32 v66, v66, v70
	v_mfma_f32_32x32x16_bf16 v[50:65], v[72:75], v[154:157], v[50:65]
	v_mul_f32_e64 v2, v2, v66
	v_mul_f32_e64 v3, v3, v66
	v_mul_f32_e64 v18, v18, v66
	v_mul_f32_e64 v19, v19, v66
	v_mul_f32_e64 v4, v4, v66
	v_mul_f32_e64 v5, v5, v66
	v_pk_mul_f32 v[20:21], v[20:21], v[66:67] op_sel_hi:[1,0]
	v_pk_mul_f32 v[70:71], v[24:25], v[66:67] op_sel_hi:[1,0]
	v_pk_fma_f32 v[24:25], v[34:35], v[68:69], v[2:3] op_sel_hi:[1,0,1] neg_lo:[0,0,1] neg_hi:[0,0,1]
	v_pk_mul_f32 v[72:73], v[26:27], v[66:67] op_sel_hi:[1,0]
	s_nop 1
	v_pk_fma_f32 v[2:3], v[50:51], v[68:69], v[18:19] op_sel_hi:[1,0,1] neg_lo:[0,0,1] neg_hi:[0,0,1]
	v_pk_fma_f32 v[26:27], v[36:37], v[68:69], v[4:5] op_sel_hi:[1,0,1] neg_lo:[0,0,1] neg_hi:[0,0,1]
	v_pk_fma_f32 v[4:5], v[52:53], v[68:69], v[20:21] op_sel_hi:[1,0,1] neg_lo:[0,0,1] neg_hi:[0,0,1]
	v_pk_mul_f32 v[18:19], v[2:3], v[2:3]
	v_pk_mul_f32 v[6:7], v[6:7], v[66:67] op_sel_hi:[1,0]
	v_pk_mul_f32 v[22:23], v[22:23], v[66:67] op_sel_hi:[1,0]
	v_pk_mul_f32 v[36:37], v[4:5], v[4:5]
	v_pk_fma_f32 v[18:19], v[24:25], v[24:25], v[18:19]
	v_pk_mul_f32 v[74:75], v[28:29], v[66:67] op_sel_hi:[1,0]
	v_pk_fma_f32 v[28:29], v[38:39], v[68:69], v[6:7] op_sel_hi:[1,0,1] neg_lo:[0,0,1] neg_hi:[0,0,1]
	v_pk_fma_f32 v[6:7], v[54:55], v[68:69], v[22:23] op_sel_hi:[1,0,1] neg_lo:[0,0,1] neg_hi:[0,0,1]
	v_pk_fma_f32 v[36:37], v[26:27], v[26:27], v[36:37]
	v_add_f32_e32 v18, v18, v19
	v_pk_mul_f32 v[8:9], v[8:9], v[66:67] op_sel_hi:[1,0]
	v_pk_mul_f32 v[38:39], v[6:7], v[6:7]
	v_add_f32_e32 v18, v36, v18
	v_pk_mul_f32 v[76:77], v[30:31], v[66:67] op_sel_hi:[1,0]
	v_pk_fma_f32 v[30:31], v[40:41], v[68:69], v[8:9] op_sel_hi:[1,0,1] neg_lo:[0,0,1] neg_hi:[0,0,1]
	v_pk_fma_f32 v[8:9], v[56:57], v[68:69], v[70:71] op_sel_hi:[1,0,1] neg_lo:[0,0,1] neg_hi:[0,0,1]
	v_pk_fma_f32 v[38:39], v[28:29], v[28:29], v[38:39]
	v_add_f32_e32 v18, v37, v18
	v_pk_mul_f32 v[10:11], v[10:11], v[66:67] op_sel_hi:[1,0]
	v_pk_mul_f32 v[40:41], v[8:9], v[8:9]
	v_add_f32_e32 v18, v38, v18
	v_pk_mul_f32 v[78:79], v[32:33], v[66:67] op_sel_hi:[1,0]
	v_pk_fma_f32 v[32:33], v[42:43], v[68:69], v[10:11] op_sel_hi:[1,0,1] neg_lo:[0,0,1] neg_hi:[0,0,1]
	v_pk_fma_f32 v[10:11], v[58:59], v[68:69], v[72:73] op_sel_hi:[1,0,1] neg_lo:[0,0,1] neg_hi:[0,0,1]
	v_pk_fma_f32 v[40:41], v[30:31], v[30:31], v[40:41]
	v_add_f32_e32 v18, v39, v18
	v_pk_mul_f32 v[12:13], v[12:13], v[66:67] op_sel_hi:[1,0]
	v_pk_mul_f32 v[42:43], v[10:11], v[10:11]
	v_add_f32_e32 v18, v40, v18
	v_pk_fma_f32 v[34:35], v[44:45], v[68:69], v[12:13] op_sel_hi:[1,0,1] neg_lo:[0,0,1] neg_hi:[0,0,1]
	v_pk_fma_f32 v[12:13], v[60:61], v[68:69], v[74:75] op_sel_hi:[1,0,1] neg_lo:[0,0,1] neg_hi:[0,0,1]
	v_pk_fma_f32 v[42:43], v[32:33], v[32:33], v[42:43]
	v_add_f32_e32 v18, v41, v18
	v_pk_mul_f32 v[14:15], v[14:15], v[66:67] op_sel_hi:[1,0]
	v_pk_mul_f32 v[44:45], v[12:13], v[12:13]
	v_add_f32_e32 v18, v42, v18
	v_pk_fma_f32 v[20:21], v[46:47], v[68:69], v[14:15] op_sel_hi:[1,0,1] neg_lo:[0,0,1] neg_hi:[0,0,1]
	v_pk_fma_f32 v[14:15], v[62:63], v[68:69], v[76:77] op_sel_hi:[1,0,1] neg_lo:[0,0,1] neg_hi:[0,0,1]
	v_pk_fma_f32 v[44:45], v[34:35], v[34:35], v[44:45]
	v_add_f32_e32 v18, v43, v18
	v_pk_mul_f32 v[16:17], v[16:17], v[66:67] op_sel_hi:[1,0]
	v_pk_mul_f32 v[46:47], v[14:15], v[14:15]
	v_add_f32_e32 v18, v44, v18
	v_pk_fma_f32 v[22:23], v[48:49], v[68:69], v[16:17] op_sel_hi:[1,0,1] neg_lo:[0,0,1] neg_hi:[0,0,1]
	v_pk_fma_f32 v[16:17], v[64:65], v[68:69], v[78:79] op_sel_hi:[1,0,1] neg_lo:[0,0,1] neg_hi:[0,0,1]
	v_pk_fma_f32 v[46:47], v[20:21], v[20:21], v[46:47]
	v_add_f32_e32 v18, v45, v18
	v_pk_mul_f32 v[48:49], v[16:17], v[16:17]
	v_add_f32_e32 v18, v46, v18
	v_pk_fma_f32 v[48:49], v[22:23], v[22:23], v[48:49]
	v_add_f32_e32 v18, v47, v18
	v_add_f32_e32 v18, v48, v18
	v_add_f32_e32 v36, v49, v18
	v_xor_b32_e32 v18, 0x80, v69
	ds_bpermute_b32 v37, v18, v36
	s_cbranch_scc0 .LBB0_951
	s_waitcnt lgkmcnt(0)
	v_add_f32_e32 v36, v36, v37
	v_fmamk_f32 v36, v36, 0x3c800000, v224
	v_cmp_gt_f32_e32 vcc, s31, v36
	v_mul_f32_e32 v37, 0x4b800000, v36
	v_and_or_b32 v18, v0, 31, s21
	v_cndmask_b32_e32 v36, v36, v37, vcc
	v_rsq_f32_e32 v36, v36
	v_lshrrev_b32_e32 v0, 3, v0
	v_and_b32_e32 v0, 4, v0
	v_lshlrev_b32_e32 v41, 2, v0
	v_mul_f32_e32 v37, 0x45800000, v36
	v_cndmask_b32_e32 v36, v36, v37, vcc
	v_mul_f32_e32 v40, v67, v36
	global_load_dwordx4 v[36:39], v41, s[8:9] offset:128
	s_lshl_b64 s[10:11], s[10:11], 11
	s_add_u32 s10, s2, s10
	s_addc_u32 s11, s3, s11
	s_lshl_b32 s20, s20, 1
	s_add_u32 s10, s10, s20
	v_ashrrev_i32_e32 v19, 31, v18
	s_addc_u32 s11, s11, 0
	v_lshlrev_b64 v[18:19], 11, v[18:19]
	v_lshl_add_u64 v[18:19], s[10:11], 0, v[18:19]
	v_lshlrev_b32_e32 v0, 1, v0
	v_lshl_add_u64 v[18:19], v[18:19], 0, v[0:1]
	s_waitcnt vmcnt(0)
	v_pk_mul_f32 v[36:37], v[40:41], v[36:37] op_sel_hi:[0,1]
	v_pk_mul_f32 v[2:3], v[2:3], v[36:37]
	v_pk_mul_f32 v[36:37], v[40:41], v[38:39] op_sel_hi:[0,1]
	v_pk_mul_f32 v[4:5], v[4:5], v[36:37]
	global_load_dwordx4 v[36:39], v41, s[8:9] offset:160
	v_cvt_pk_bf16_f32 v2, v2, v3
	v_cvt_pk_bf16_f32 v3, v4, v5
	s_waitcnt vmcnt(0)
	v_pk_mul_f32 v[36:37], v[40:41], v[36:37] op_sel_hi:[0,1]
	v_pk_mul_f32 v[6:7], v[6:7], v[36:37]
	v_pk_mul_f32 v[36:37], v[40:41], v[38:39] op_sel_hi:[0,1]
	v_pk_mul_f32 v[8:9], v[8:9], v[36:37]
	global_load_dwordx4 v[36:39], v41, s[8:9] offset:192
	v_cvt_pk_bf16_f32 v4, v6, v7
	v_cvt_pk_bf16_f32 v5, v8, v9
	s_waitcnt vmcnt(0)
	v_pk_mul_f32 v[36:37], v[40:41], v[36:37] op_sel_hi:[0,1]
	v_pk_mul_f32 v[10:11], v[10:11], v[36:37]
	v_pk_mul_f32 v[36:37], v[40:41], v[38:39] op_sel_hi:[0,1]
	v_pk_mul_f32 v[12:13], v[12:13], v[36:37]
	global_load_dwordx4 v[36:39], v41, s[8:9] offset:224
	s_waitcnt vmcnt(0)
	v_pk_mul_f32 v[36:37], v[40:41], v[36:37] op_sel_hi:[0,1]
	v_pk_mul_f32 v[14:15], v[14:15], v[36:37]
	v_pk_mul_f32 v[36:37], v[40:41], v[38:39] op_sel_hi:[0,1]
	v_pk_mul_f32 v[16:17], v[16:17], v[36:37]
	global_load_dwordx4 v[36:39], v41, s[8:9]
	s_waitcnt vmcnt(0)
	v_pk_mul_f32 v[36:37], v[40:41], v[36:37] op_sel_hi:[0,1]
	v_pk_mul_f32 v[24:25], v[24:25], v[36:37]
	v_pk_mul_f32 v[36:37], v[40:41], v[38:39] op_sel_hi:[0,1]
	v_pk_mul_f32 v[26:27], v[26:27], v[36:37]
	global_load_dwordx4 v[36:39], v41, s[8:9] offset:32
	v_cvt_pk_bf16_f32 v24, v24, v25
	v_cvt_pk_bf16_f32 v25, v26, v27
	s_waitcnt vmcnt(0)
	v_pk_mul_f32 v[36:37], v[40:41], v[36:37] op_sel_hi:[0,1]
	v_pk_mul_f32 v[28:29], v[28:29], v[36:37]
	v_pk_mul_f32 v[36:37], v[40:41], v[38:39] op_sel_hi:[0,1]
	v_pk_mul_f32 v[30:31], v[30:31], v[36:37]
	global_load_dwordx4 v[36:39], v41, s[8:9] offset:64
	s_waitcnt vmcnt(0)
	v_pk_mul_f32 v[36:37], v[40:41], v[36:37] op_sel_hi:[0,1]
	v_pk_mul_f32 v[32:33], v[32:33], v[36:37]
	v_pk_mul_f32 v[36:37], v[40:41], v[38:39] op_sel_hi:[0,1]
	v_pk_mul_f32 v[34:35], v[34:35], v[36:37]
	global_load_dwordx4 v[36:39], v41, s[8:9] offset:96
	s_nop 0
	global_store_dwordx2 v[18:19], v[24:25], off offset:1024
	global_store_dwordx2 v[18:19], v[2:3], off offset:1088
	v_cvt_pk_bf16_f32 v2, v28, v29
	v_cvt_pk_bf16_f32 v3, v30, v31
	global_store_dwordx2 v[18:19], v[2:3], off offset:1040
	global_store_dwordx2 v[18:19], v[4:5], off offset:1104
	v_cvt_pk_bf16_f32 v2, v32, v33
	v_cvt_pk_bf16_f32 v3, v34, v35
	v_cvt_pk_bf16_f32 v4, v10, v11
	v_cvt_pk_bf16_f32 v5, v12, v13
	global_store_dwordx2 v[18:19], v[2:3], off offset:1056
	global_store_dwordx2 v[18:19], v[4:5], off offset:1120
	v_cvt_pk_bf16_f32 v4, v14, v15
	v_cvt_pk_bf16_f32 v5, v16, v17
	s_waitcnt vmcnt(6)
	v_pk_mul_f32 v[36:37], v[40:41], v[36:37] op_sel_hi:[0,1]
	v_pk_mul_f32 v[20:21], v[20:21], v[36:37]
	v_pk_mul_f32 v[36:37], v[40:41], v[38:39] op_sel_hi:[0,1]
	v_pk_mul_f32 v[22:23], v[22:23], v[36:37]
	v_cvt_pk_bf16_f32 v2, v20, v21
	v_cvt_pk_bf16_f32 v3, v22, v23
	global_store_dwordx2 v[18:19], v[2:3], off offset:1072
	global_store_dwordx2 v[18:19], v[4:5], off offset:1136
	s_branch .LBB0_951
